# retention prefix-scan loop: 17 state loads hoisted ahead of the dependent fma/store chain
# speedup vs baseline: 1.0058x; 1.0011x over previous
.LBB0_595:
	v_ashrrev_i32_e32 v4, 12, v1
	v_lshlrev_b32_e32 v2, 2, v4
	v_bfe_u32 v0, v1, 13, 2
	v_and_b32_e32 v2, 4, v2
	v_or3_b32 v96, v0, v2, s30
	v_lshl_add_u64 v[2:3], v[96:97], 2, s[6:7]
	global_load_dword v0, v[2:3], off
	v_mul_i32_i24_e32 v2, 18, v4
	v_ashrrev_i32_e32 v3, 31, v2
	v_and_b32_e32 v7, 0x3ffc, v6
	v_lshlrev_b64 v[4:5], 16, v[2:3]
	v_lshl_add_u64 v[4:5], s[8:9], 0, v[4:5]
	v_lshlrev_b32_e32 v96, 2, v7
	v_lshlrev_b64 v[2:3], 15, v[2:3]
	v_lshl_add_u64 v[4:5], v[4:5], 0, v[96:97]
	v_lshl_add_u64 v[2:3], s[10:11], 0, v[2:3]
	v_lshlrev_b32_e32 v96, 1, v7
	v_lshl_add_u64 v[2:3], v[2:3], 0, v[96:97]
	v_mov_b32_e32 v7, v97
	s_mov_b32 s0, 0x18000
	v_cvt_pk_bf16_f32 v8, v7, v7
	v_cvt_pk_bf16_f32 v9, v7, v7
	global_store_dwordx2 v[2:3], v[8:9], off
	global_load_dwordx4 v[100:103], v[4:5], off
	v_add_co_u32_e32 v168, vcc, 0x10000, v4
	s_nop 1
	v_addc_co_u32_e32 v169, vcc, 0, v5, vcc
	global_load_dwordx4 v[104:107], v[168:169], off
	v_add_co_u32_e32 v168, vcc, 0x20000, v4
	s_nop 1
	v_addc_co_u32_e32 v169, vcc, 0, v5, vcc
	global_load_dwordx4 v[108:111], v[168:169], off
	v_add_co_u32_e32 v168, vcc, 0x30000, v4
	s_nop 1
	v_addc_co_u32_e32 v169, vcc, 0, v5, vcc
	global_load_dwordx4 v[112:115], v[168:169], off
	v_add_co_u32_e32 v168, vcc, 0x40000, v4
	s_nop 1
	v_addc_co_u32_e32 v169, vcc, 0, v5, vcc
	global_load_dwordx4 v[116:119], v[168:169], off
	v_add_co_u32_e32 v168, vcc, 0x50000, v4
	s_nop 1
	v_addc_co_u32_e32 v169, vcc, 0, v5, vcc
	global_load_dwordx4 v[120:123], v[168:169], off
	v_add_co_u32_e32 v168, vcc, 0x60000, v4
	s_nop 1
	v_addc_co_u32_e32 v169, vcc, 0, v5, vcc
	global_load_dwordx4 v[124:127], v[168:169], off
	v_add_co_u32_e32 v168, vcc, 0x70000, v4
	s_nop 1
	v_addc_co_u32_e32 v169, vcc, 0, v5, vcc
	global_load_dwordx4 v[128:131], v[168:169], off
	v_add_co_u32_e32 v168, vcc, 0x80000, v4
	s_nop 1
	v_addc_co_u32_e32 v169, vcc, 0, v5, vcc
	global_load_dwordx4 v[132:135], v[168:169], off
	v_add_co_u32_e32 v168, vcc, 0x90000, v4
	s_nop 1
	v_addc_co_u32_e32 v169, vcc, 0, v5, vcc
	global_load_dwordx4 v[136:139], v[168:169], off
	v_add_co_u32_e32 v168, vcc, 0xa0000, v4
	s_nop 1
	v_addc_co_u32_e32 v169, vcc, 0, v5, vcc
	global_load_dwordx4 v[140:143], v[168:169], off
	v_add_co_u32_e32 v168, vcc, 0xb0000, v4
	s_nop 1
	v_addc_co_u32_e32 v169, vcc, 0, v5, vcc
	global_load_dwordx4 v[144:147], v[168:169], off
	v_add_co_u32_e32 v168, vcc, 0xc0000, v4
	s_nop 1
	v_addc_co_u32_e32 v169, vcc, 0, v5, vcc
	global_load_dwordx4 v[148:151], v[168:169], off
	v_add_co_u32_e32 v168, vcc, 0xd0000, v4
	s_nop 1
	v_addc_co_u32_e32 v169, vcc, 0, v5, vcc
	global_load_dwordx4 v[152:155], v[168:169], off
	v_add_co_u32_e32 v168, vcc, 0xe0000, v4
	s_nop 1
	v_addc_co_u32_e32 v169, vcc, 0, v5, vcc
	global_load_dwordx4 v[156:159], v[168:169], off
	v_add_co_u32_e32 v168, vcc, 0xf0000, v4
	s_nop 1
	v_addc_co_u32_e32 v169, vcc, 0, v5, vcc
	global_load_dwordx4 v[160:163], v[168:169], off
	v_add_co_u32_e32 v168, vcc, 0x100000, v4
	s_nop 1
	v_addc_co_u32_e32 v169, vcc, 0, v5, vcc
	global_load_dwordx4 v[164:167], v[168:169], off
	v_add_u32_e32 v6, s16, v6
	s_waitcnt vmcnt(17)
	v_mul_f32_e32 v0, 0x43000000, v0
	v_exp_f32_e32 v0, v0
	s_waitcnt vmcnt(16)
	v_mov_b32_e32 v12, v100
	v_mov_b32_e32 v13, v101
	v_mov_b32_e32 v14, v102
	v_mov_b32_e32 v15, v103
	v_add_co_u32_e32 v10, vcc, 0x8000, v2
	v_cvt_pk_bf16_f32 v8, v12, v13
	v_cvt_pk_bf16_f32 v9, v14, v15
	v_addc_co_u32_e32 v11, vcc, 0, v3, vcc
	global_store_dwordx2 v[10:11], v[8:9], off
	s_waitcnt vmcnt(16)
	v_fma_f32 v12, v0, v12, v104
	v_fma_f32 v13, v0, v13, v105
	v_fma_f32 v14, v0, v14, v106
	v_fma_f32 v15, v0, v15, v107
	v_add_co_u32_e32 v10, vcc, 0x10000, v2
	v_cvt_pk_bf16_f32 v8, v12, v13
	v_cvt_pk_bf16_f32 v9, v14, v15
	v_addc_co_u32_e32 v11, vcc, 0, v3, vcc
	global_store_dwordx2 v[10:11], v[8:9], off
	s_waitcnt vmcnt(16)
	v_fma_f32 v12, v0, v12, v108
	v_fma_f32 v13, v0, v13, v109
	v_fma_f32 v14, v0, v14, v110
	v_fma_f32 v15, v0, v15, v111
	v_add_co_u32_e32 v10, vcc, 0x18000, v2
	v_cvt_pk_bf16_f32 v8, v12, v13
	v_cvt_pk_bf16_f32 v9, v14, v15
	v_addc_co_u32_e32 v11, vcc, 0, v3, vcc
	global_store_dwordx2 v[10:11], v[8:9], off
	s_waitcnt vmcnt(16)
	v_fma_f32 v12, v0, v12, v112
	v_fma_f32 v13, v0, v13, v113
	v_fma_f32 v14, v0, v14, v114
	v_fma_f32 v15, v0, v15, v115
	v_add_co_u32_e32 v10, vcc, 0x20000, v2
	v_cvt_pk_bf16_f32 v8, v12, v13
	v_cvt_pk_bf16_f32 v9, v14, v15
	v_addc_co_u32_e32 v11, vcc, 0, v3, vcc
	global_store_dwordx2 v[10:11], v[8:9], off
	s_waitcnt vmcnt(16)
	v_fma_f32 v12, v0, v12, v116
	v_fma_f32 v13, v0, v13, v117
	v_fma_f32 v14, v0, v14, v118
	v_fma_f32 v15, v0, v15, v119
	v_add_co_u32_e32 v10, vcc, 0x28000, v2
	v_cvt_pk_bf16_f32 v8, v12, v13
	v_cvt_pk_bf16_f32 v9, v14, v15
	v_addc_co_u32_e32 v11, vcc, 0, v3, vcc
	global_store_dwordx2 v[10:11], v[8:9], off
	s_waitcnt vmcnt(16)
	v_fma_f32 v12, v0, v12, v120
	v_fma_f32 v13, v0, v13, v121
	v_fma_f32 v14, v0, v14, v122
	v_fma_f32 v15, v0, v15, v123
	v_add_co_u32_e32 v10, vcc, 0x30000, v2
	v_cvt_pk_bf16_f32 v8, v12, v13
	v_cvt_pk_bf16_f32 v9, v14, v15
	v_addc_co_u32_e32 v11, vcc, 0, v3, vcc
	global_store_dwordx2 v[10:11], v[8:9], off
	s_waitcnt vmcnt(16)
	v_fma_f32 v12, v0, v12, v124
	v_fma_f32 v13, v0, v13, v125
	v_fma_f32 v14, v0, v14, v126
	v_fma_f32 v15, v0, v15, v127
	v_add_co_u32_e32 v10, vcc, 0x38000, v2
	v_cvt_pk_bf16_f32 v8, v12, v13
	v_cvt_pk_bf16_f32 v9, v14, v15
	v_addc_co_u32_e32 v11, vcc, 0, v3, vcc
	global_store_dwordx2 v[10:11], v[8:9], off
	s_waitcnt vmcnt(16)
	v_fma_f32 v12, v0, v12, v128
	v_fma_f32 v13, v0, v13, v129
	v_fma_f32 v14, v0, v14, v130
	v_fma_f32 v15, v0, v15, v131
	v_add_co_u32_e32 v10, vcc, 0x40000, v2
	v_cvt_pk_bf16_f32 v8, v12, v13
	v_cvt_pk_bf16_f32 v9, v14, v15
	v_addc_co_u32_e32 v11, vcc, 0, v3, vcc
	global_store_dwordx2 v[10:11], v[8:9], off
	s_waitcnt vmcnt(16)
	v_fma_f32 v12, v0, v12, v132
	v_fma_f32 v13, v0, v13, v133
	v_fma_f32 v14, v0, v14, v134
	v_fma_f32 v15, v0, v15, v135
	v_add_co_u32_e32 v10, vcc, 0x48000, v2
	v_cvt_pk_bf16_f32 v8, v12, v13
	v_cvt_pk_bf16_f32 v9, v14, v15
	v_addc_co_u32_e32 v11, vcc, 0, v3, vcc
	global_store_dwordx2 v[10:11], v[8:9], off
	s_waitcnt vmcnt(16)
	v_fma_f32 v12, v0, v12, v136
	v_fma_f32 v13, v0, v13, v137
	v_fma_f32 v14, v0, v14, v138
	v_fma_f32 v15, v0, v15, v139
	v_add_co_u32_e32 v10, vcc, 0x50000, v2
	v_cvt_pk_bf16_f32 v8, v12, v13
	v_cvt_pk_bf16_f32 v9, v14, v15
	v_addc_co_u32_e32 v11, vcc, 0, v3, vcc
	global_store_dwordx2 v[10:11], v[8:9], off
	s_waitcnt vmcnt(16)
	v_fma_f32 v12, v0, v12, v140
	v_fma_f32 v13, v0, v13, v141
	v_fma_f32 v14, v0, v14, v142
	v_fma_f32 v15, v0, v15, v143
	v_add_co_u32_e32 v10, vcc, 0x58000, v2
	v_cvt_pk_bf16_f32 v8, v12, v13
	v_cvt_pk_bf16_f32 v9, v14, v15
	v_addc_co_u32_e32 v11, vcc, 0, v3, vcc
	global_store_dwordx2 v[10:11], v[8:9], off
	s_waitcnt vmcnt(16)
	v_fma_f32 v12, v0, v12, v144
	v_fma_f32 v13, v0, v13, v145
	v_fma_f32 v14, v0, v14, v146
	v_fma_f32 v15, v0, v15, v147
	v_add_co_u32_e32 v10, vcc, 0x60000, v2
	v_cvt_pk_bf16_f32 v8, v12, v13
	v_cvt_pk_bf16_f32 v9, v14, v15
	v_addc_co_u32_e32 v11, vcc, 0, v3, vcc
	global_store_dwordx2 v[10:11], v[8:9], off
	s_waitcnt vmcnt(16)
	v_fma_f32 v12, v0, v12, v148
	v_fma_f32 v13, v0, v13, v149
	v_fma_f32 v14, v0, v14, v150
	v_fma_f32 v15, v0, v15, v151
	v_add_co_u32_e32 v10, vcc, 0x68000, v2
	v_cvt_pk_bf16_f32 v8, v12, v13
	v_cvt_pk_bf16_f32 v9, v14, v15
	v_addc_co_u32_e32 v11, vcc, 0, v3, vcc
	global_store_dwordx2 v[10:11], v[8:9], off
	s_waitcnt vmcnt(16)
	v_fma_f32 v12, v0, v12, v152
	v_fma_f32 v13, v0, v13, v153
	v_fma_f32 v14, v0, v14, v154
	v_fma_f32 v15, v0, v15, v155
	v_add_co_u32_e32 v10, vcc, 0x70000, v2
	v_cvt_pk_bf16_f32 v8, v12, v13
	v_cvt_pk_bf16_f32 v9, v14, v15
	v_addc_co_u32_e32 v11, vcc, 0, v3, vcc
	global_store_dwordx2 v[10:11], v[8:9], off
	s_waitcnt vmcnt(16)
	v_fma_f32 v12, v0, v12, v156
	v_fma_f32 v13, v0, v13, v157
	v_fma_f32 v14, v0, v14, v158
	v_fma_f32 v15, v0, v15, v159
	v_add_co_u32_e32 v10, vcc, 0x78000, v2
	v_cvt_pk_bf16_f32 v8, v12, v13
	v_cvt_pk_bf16_f32 v9, v14, v15
	v_addc_co_u32_e32 v11, vcc, 0, v3, vcc
	global_store_dwordx2 v[10:11], v[8:9], off
	s_waitcnt vmcnt(16)
	v_fma_f32 v12, v0, v12, v160
	v_fma_f32 v13, v0, v13, v161
	v_fma_f32 v14, v0, v14, v162
	v_fma_f32 v15, v0, v15, v163
	v_add_co_u32_e32 v10, vcc, 0x80000, v2
	v_cvt_pk_bf16_f32 v8, v12, v13
	v_cvt_pk_bf16_f32 v9, v14, v15
	v_addc_co_u32_e32 v11, vcc, 0, v3, vcc
	global_store_dwordx2 v[10:11], v[8:9], off
	s_waitcnt vmcnt(16)
	v_fma_f32 v12, v0, v12, v164
	v_fma_f32 v13, v0, v13, v165
	v_fma_f32 v14, v0, v14, v166
	v_fma_f32 v15, v0, v15, v167
	v_add_co_u32_e32 v10, vcc, 0x88000, v2
	v_cvt_pk_bf16_f32 v8, v12, v13
	v_cvt_pk_bf16_f32 v9, v14, v15
	v_addc_co_u32_e32 v11, vcc, 0, v3, vcc
	global_store_dwordx2 v[10:11], v[8:9], off
	v_add_u32_e32 v1, s14, v1
	v_cmp_lt_i32_e32 vcc, 0x3ffff, v1
	s_or_b64 s[12:13], vcc, s[12:13]
	s_andn2_b64 exec, exec, s[12:13]
	s_cbranch_execnz .LBB0_595
